# v21 + router job's double-cost prologue tiles shifted onto the waves that otherwise get 7 tiles
# speedup vs baseline: 1.0022x; 1.0022x over previous
; DI void phase_prologue(const Ctx& c) {
;     ...
;         const int tk = jb.K / 64, tn = jb.N / 64, per = tk * tn, total = jb.count * per;
;         for (int t = gw; t < total; t += nw) {
;             const int mi = t / per, r = t % per, kt = r / tn, ntl = r % tn;
.LBB0_39:
	s_lshr_b32 s65, s22, 6
	s_lshr_b32 s73, s72, 6
	s_mul_i32 s74, s73, s65
	s_mul_i32 s75, s74, s64
	s_cmp_eq_u32 s33, 9
	s_cselect_b32 s94, 64, 0
	s_add_i32 s94, s94, s95
	s_sub_i32 s94, s1, s94
	s_and_b32 s94, s94, 0x7ff
	s_add_i32 s95, s95, s75
	s_cmp_ge_i32 s94, s75
	s_cbranch_scc1 .LBB0_5
	v_cvt_f32_u32_e32 v16, s74
	v_cvt_f32_u32_e32 v17, s73
	s_sub_i32 s68, 0, s74
	s_sub_i32 s69, 0, s73
	v_rcp_iflag_f32_e32 v16, v16
	v_rcp_iflag_f32_e32 v17, v17
	s_mul_i32 s64, s72, s22
	s_mov_b32 s65, s23
	v_mul_f32_e32 v16, 0x4f7ffffe, v16
	v_mul_f32_e32 v17, 0x4f7ffffe, v17
	v_cvt_u32_f32_e32 v16, v16
	v_cvt_u32_f32_e32 v17, v17
	v_readfirstlane_b32 s70, v16
	v_readfirstlane_b32 s71, v17
	s_mul_i32 s68, s68, s70
	s_mul_hi_u32 s68, s70, s68
	s_mul_i32 s69, s69, s71
	s_add_i32 s76, s70, s68
	s_mul_hi_u32 s68, s71, s69
	s_add_i32 s77, s71, s68
	v_lshl_add_u64 v[16:17], s[66:67], 0, v[0:1]
	s_lshl_b64 s[66:67], s[64:65], 1
	s_lshl_b64 s[68:69], s[22:23], 6
	s_mov_b32 s65, s94
	s_branch .LBB0_42
